# combination of the two size-neutral K-loop edits: mid-segment s_setprio flips removed and loop-control SALU hoisted before the closing barrier
# baseline (speedup 1.0000x reference)
.Lpeel1f_sub3:
	s_add_i32 s75, 0, 0x18000
	s_add_i32 s76, 0, 0x1c000
	v_add_u32_e32 v12, s75, v182
	v_add_u32_e32 v28, s76, v182
	ds_read_b128 v[0:3], v12
	ds_read_b128 v[4:7], v12 offset:1024
	ds_read_b128 v[8:11], v12 offset:2048
	ds_read_b128 v[12:15], v12 offset:3072
	ds_read_b128 v[16:19], v28
	ds_read_b128 v[20:23], v28 offset:1024
	ds_read_b128 v[24:27], v28 offset:2048
	ds_read_b128 v[28:31], v28 offset:3072
	s_add_u32 s10, s10, 0x40000
	s_addc_u32 s11, s11, 0
	s_mov_b32 m0, s85
	v_lshl_add_u64 v[220:221], s[10:11], 0, v[160:161]
	ds_read_b128 v[188:191], v185 offset:32768
	ds_read_b128 v[192:195], v185 offset:33792
	ds_read_b128 v[196:199], v185 offset:34816
	ds_read_b128 v[200:203], v185 offset:35840
	ds_read_b128 v[204:207], v185 offset:36864
	ds_read_b128 v[208:211], v185 offset:37888
	ds_read_b128 v[212:215], v185 offset:38912
	ds_read_b128 v[216:219], v185 offset:39936
	global_load_lds_dwordx4 v[220:221], off
	v_lshl_add_u64 v[220:221], s[10:11], 0, v[164:165]
	s_mov_b32 m0, s86
	s_nop 0
	global_load_lds_dwordx4 v[220:221], off
	s_waitcnt vmcnt(8)
	s_waitcnt lgkmcnt(0)
	s_barrier
	s_setprio 1
	s_waitcnt lgkmcnt(0)
	v_mfma_f32_16x16x128_f8f6f4 v[156:159], v[0:7], v[188:195], v[156:159]
	v_mfma_f32_16x16x128_f8f6f4 v[152:155], v[8:15], v[188:195], v[152:155]
	v_mfma_f32_16x16x128_f8f6f4 v[140:143], v[0:7], v[196:203], v[140:143]
	v_mfma_f32_16x16x128_f8f6f4 v[136:139], v[8:15], v[196:203], v[136:139]
	v_mfma_f32_16x16x128_f8f6f4 v[124:127], v[0:7], v[204:211], v[124:127]
	v_mfma_f32_16x16x128_f8f6f4 v[120:123], v[8:15], v[204:211], v[120:123]
	v_mfma_f32_16x16x128_f8f6f4 v[108:111], v[0:7], v[212:219], v[108:111]
	v_mfma_f32_16x16x128_f8f6f4 v[104:107], v[8:15], v[212:219], v[104:107]
	v_mfma_f32_16x16x128_f8f6f4 v[148:151], v[16:23], v[188:195], v[148:151]
	v_mfma_f32_16x16x128_f8f6f4 v[144:147], v[24:31], v[188:195], v[144:147]
	v_mfma_f32_16x16x128_f8f6f4 v[132:135], v[16:23], v[196:203], v[132:135]
	v_mfma_f32_16x16x128_f8f6f4 v[128:131], v[24:31], v[196:203], v[128:131]
	v_mfma_f32_16x16x128_f8f6f4 v[116:119], v[16:23], v[204:211], v[116:119]
	v_mfma_f32_16x16x128_f8f6f4 v[112:115], v[24:31], v[204:211], v[112:115]
	v_mfma_f32_16x16x128_f8f6f4 v[100:103], v[16:23], v[212:219], v[100:103]
	v_mfma_f32_16x16x128_f8f6f4 v[96:99], v[24:31], v[212:219], v[96:99]
	s_setprio 0
	s_nop 0
	s_nop 0
	s_barrier
	s_add_i32 s10, s75, s38
	v_lshl_add_u64 v[174:175], v[174:175], 0, s[42:43]
	s_mov_b32 m0, s10
	ds_read_b128 v[188:191], v185 offset:49152
	ds_read_b128 v[192:195], v185 offset:50176
	ds_read_b128 v[196:199], v185 offset:51200
	ds_read_b128 v[200:203], v185 offset:52224
	ds_read_b128 v[204:207], v185 offset:53248
	ds_read_b128 v[208:211], v185 offset:54272
	ds_read_b128 v[212:215], v185 offset:55296
	ds_read_b128 v[216:219], v185 offset:56320
	global_load_lds_dwordx4 v[174:175], off
	s_add_i32 m0, s10, 0x2000
	s_add_u32 s8, s8, 0x40080
	v_lshl_add_u64 v[174:175], v[176:177], 0, s[42:43]
	s_addc_u32 s9, s9, 0
	s_add_i32 s10, s76, s38
	global_load_lds_dwordx4 v[174:175], off
	v_lshl_add_u64 v[174:175], s[8:9], 0, v[162:163]
	s_mov_b32 m0, s10
	s_nop 0
	global_load_lds_dwordx4 v[174:175], off
	v_lshl_add_u64 v[174:175], s[8:9], 0, v[166:167]
	s_add_i32 m0, s10, 0x2000
	s_nop 0
	global_load_lds_dwordx4 v[174:175], off
	v_lshl_add_u64 v[174:175], v[178:179], 0, s[42:43]
	s_mov_b32 m0, s87
	s_nop 0
	global_load_lds_dwordx4 v[174:175], off
	v_lshl_add_u64 v[174:175], v[180:181], 0, s[42:43]
	s_mov_b32 m0, s88
	s_nop 0
	global_load_lds_dwordx4 v[174:175], off
	s_waitcnt vmcnt(8)
	s_waitcnt lgkmcnt(0)
	s_barrier
	s_setprio 1
	s_waitcnt lgkmcnt(0)
	v_mfma_f32_16x16x128_f8f6f4 v[92:95], v[0:7], v[188:195], v[92:95]
	v_mfma_f32_16x16x128_f8f6f4 v[88:91], v[8:15], v[188:195], v[88:91]
	v_mfma_f32_16x16x128_f8f6f4 v[76:79], v[0:7], v[196:203], v[76:79]
	v_mfma_f32_16x16x128_f8f6f4 v[72:75], v[8:15], v[196:203], v[72:75]
	v_mfma_f32_16x16x128_f8f6f4 v[60:63], v[0:7], v[204:211], v[60:63]
	v_mfma_f32_16x16x128_f8f6f4 v[56:59], v[8:15], v[204:211], v[56:59]
	v_mfma_f32_16x16x128_f8f6f4 v[44:47], v[0:7], v[212:219], v[44:47]
	v_mfma_f32_16x16x128_f8f6f4 v[40:43], v[8:15], v[212:219], v[40:43]
	v_mfma_f32_16x16x128_f8f6f4 v[84:87], v[16:23], v[188:195], v[84:87]
	v_mfma_f32_16x16x128_f8f6f4 v[80:83], v[24:31], v[188:195], v[80:83]
	v_mfma_f32_16x16x128_f8f6f4 v[68:71], v[16:23], v[196:203], v[68:71]
	v_mfma_f32_16x16x128_f8f6f4 v[64:67], v[24:31], v[196:203], v[64:67]
	v_mfma_f32_16x16x128_f8f6f4 v[52:55], v[16:23], v[204:211], v[52:55]
	v_mfma_f32_16x16x128_f8f6f4 v[48:51], v[24:31], v[204:211], v[48:51]
	v_mfma_f32_16x16x128_f8f6f4 v[36:39], v[16:23], v[212:219], v[36:39]
	v_mfma_f32_16x16x128_f8f6f4 v[32:35], v[24:31], v[212:219], v[32:35]
	s_setprio 0
	s_nop 0
	s_nop 0
	s_add_i32 s74, s74, 2
	s_add_u32 s6, s6, 0x100
	s_addc_u32 s7, s7, 0
	s_add_u32 s37, s37, 0x100
	s_addc_u32 s67, s67, 0
	s_cmp_gt_u32 s74, 13
	s_barrier
	s_cbranch_scc0 .LBB0_358
	s_and_b64 vcc, exec, s[44:45]
	s_cbranch_vccz .LBB0_361
	s_barrier

.LBB0_510:
	ds_read_b128 v[24:27], v173
	ds_read_b128 v[28:31], v173 offset:1024
	ds_read_b128 v[32:35], v173 offset:2048
	ds_read_b128 v[36:39], v173 offset:3072
	ds_read_b128 v[162:165], v174
	ds_read_b128 v[166:169], v174 offset:1024
	ds_read_b128 v[178:181], v174 offset:2048
	ds_read_b128 v[182:185], v174 offset:3072
	s_add_u32 s8, s6, 0xfff80080
	s_addc_u32 s9, s7, -1
	s_cmp_eq_u32 s65, 28
	s_cselect_b32 s11, s67, s9
	s_cselect_b32 s10, s66, s8
	s_cselect_b32 s9, s69, s63
	s_cselect_b32 s8, s68, s5
	v_lshl_add_u64 v[170:171], s[6:7], 0, v[154:155]
	s_add_i32 m0, s51, 0xc000
	ds_read_b128 v[186:189], v175
	ds_read_b128 v[190:193], v175 offset:1024
	ds_read_b128 v[194:197], v175 offset:2048
	ds_read_b128 v[198:201], v175 offset:3072
	ds_read_b128 v[202:205], v175 offset:4096
	ds_read_b128 v[206:209], v175 offset:5120
	ds_read_b128 v[210:213], v175 offset:6144
	ds_read_b128 v[214:217], v175 offset:7168
	global_load_lds_dwordx4 v[170:171], off
	v_lshl_add_u64 v[170:171], s[6:7], 0, v[156:157]
	s_add_i32 m0, s51, 0xe000
	s_nop 0
	global_load_lds_dwordx4 v[170:171], off
	s_waitcnt vmcnt(8)
	s_waitcnt lgkmcnt(0)
	s_barrier
	s_setprio 1
	s_waitcnt lgkmcnt(0)
	v_mfma_f32_16x16x32_bf16 v[140:143], v[24:27], v[186:189], v[140:143]
	v_mfma_f32_16x16x32_bf16 v[136:139], v[32:35], v[186:189], v[136:139]
	v_mfma_f32_16x16x32_bf16 v[124:127], v[24:27], v[194:197], v[124:127]
	v_mfma_f32_16x16x32_bf16 v[120:123], v[32:35], v[194:197], v[120:123]
	v_mfma_f32_16x16x32_bf16 v[108:111], v[24:27], v[202:205], v[108:111]
	v_mfma_f32_16x16x32_bf16 v[104:107], v[32:35], v[202:205], v[104:107]
	v_mfma_f32_16x16x32_bf16 v[92:95], v[24:27], v[210:213], v[92:95]
	v_mfma_f32_16x16x32_bf16 v[88:91], v[32:35], v[210:213], v[88:91]
	v_mfma_f32_16x16x32_bf16 v[140:143], v[28:31], v[190:193], v[140:143]
	v_mfma_f32_16x16x32_bf16 v[136:139], v[36:39], v[190:193], v[136:139]
	v_mfma_f32_16x16x32_bf16 v[124:127], v[28:31], v[198:201], v[124:127]
	v_mfma_f32_16x16x32_bf16 v[120:123], v[36:39], v[198:201], v[120:123]
	v_mfma_f32_16x16x32_bf16 v[108:111], v[28:31], v[206:209], v[108:111]
	v_mfma_f32_16x16x32_bf16 v[104:107], v[36:39], v[206:209], v[104:107]
	v_mfma_f32_16x16x32_bf16 v[92:95], v[28:31], v[214:217], v[92:95]
	v_mfma_f32_16x16x32_bf16 v[88:91], v[36:39], v[214:217], v[88:91]
	v_mfma_f32_16x16x32_bf16 v[132:135], v[162:165], v[186:189], v[132:135]
	v_mfma_f32_16x16x32_bf16 v[128:131], v[178:181], v[186:189], v[128:131]
	v_mfma_f32_16x16x32_bf16 v[116:119], v[162:165], v[194:197], v[116:119]
	v_mfma_f32_16x16x32_bf16 v[112:115], v[178:181], v[194:197], v[112:115]
	v_mfma_f32_16x16x32_bf16 v[100:103], v[162:165], v[202:205], v[100:103]
	v_mfma_f32_16x16x32_bf16 v[96:99], v[178:181], v[202:205], v[96:99]
	v_mfma_f32_16x16x32_bf16 v[84:87], v[162:165], v[210:213], v[84:87]
	v_mfma_f32_16x16x32_bf16 v[80:83], v[178:181], v[210:213], v[80:83]
	v_mfma_f32_16x16x32_bf16 v[132:135], v[166:169], v[190:193], v[132:135]
	v_mfma_f32_16x16x32_bf16 v[128:131], v[182:185], v[190:193], v[128:131]
	v_mfma_f32_16x16x32_bf16 v[116:119], v[166:169], v[198:201], v[116:119]
	v_mfma_f32_16x16x32_bf16 v[112:115], v[182:185], v[198:201], v[112:115]
	v_mfma_f32_16x16x32_bf16 v[100:103], v[166:169], v[206:209], v[100:103]
	v_mfma_f32_16x16x32_bf16 v[96:99], v[182:185], v[206:209], v[96:99]
	v_mfma_f32_16x16x32_bf16 v[84:87], v[166:169], v[214:217], v[84:87]
	v_mfma_f32_16x16x32_bf16 v[80:83], v[182:185], v[214:217], v[80:83]
	s_setprio 0
	s_nop 0
	s_nop 0
	s_barrier
	s_add_i32 s70, s79, s38
	v_lshl_add_u64 v[170:171], s[8:9], 0, v[146:147]
	s_mov_b32 m0, s70
	ds_read_b128 v[186:189], v175 offset:16384
	ds_read_b128 v[190:193], v175 offset:17408
	ds_read_b128 v[194:197], v175 offset:18432
	ds_read_b128 v[198:201], v175 offset:19456
	ds_read_b128 v[202:205], v175 offset:20480
	ds_read_b128 v[206:209], v175 offset:21504
	ds_read_b128 v[210:213], v175 offset:22528
	ds_read_b128 v[214:217], v175 offset:23552
	global_load_lds_dwordx4 v[170:171], off
	s_add_i32 m0, s70, 0x2000
	s_add_u32 s70, s8, 0x80000
	v_lshl_add_u64 v[218:219], s[8:9], 0, v[150:151]
	s_addc_u32 s71, s9, 0
	s_add_i32 s72, s80, s38
	global_load_lds_dwordx4 v[218:219], off
	v_lshl_add_u64 v[220:221], s[70:71], 0, v[146:147]
	s_mov_b32 m0, s72
	v_lshl_add_u64 v[222:223], s[10:11], 0, v[148:149]
	global_load_lds_dwordx4 v[220:221], off
	v_lshl_add_u64 v[220:221], s[70:71], 0, v[150:151]
	s_add_i32 m0, s72, 0x2000
	s_nop 0
	global_load_lds_dwordx4 v[220:221], off
	v_lshl_add_u64 v[220:221], s[10:11], 0, v[144:145]
	s_mov_b32 m0, s51
	s_nop 0
	global_load_lds_dwordx4 v[220:221], off
	s_mov_b32 m0, s53
	s_nop 0
	global_load_lds_dwordx4 v[222:223], off
	s_waitcnt vmcnt(8)
	s_waitcnt lgkmcnt(0)
	s_barrier
	s_setprio 1
	s_waitcnt lgkmcnt(0)
	v_mfma_f32_16x16x32_bf16 v[76:79], v[24:27], v[186:189], v[76:79]
	v_mfma_f32_16x16x32_bf16 v[72:75], v[32:35], v[186:189], v[72:75]
	v_mfma_f32_16x16x32_bf16 v[60:63], v[24:27], v[194:197], v[60:63]
	v_mfma_f32_16x16x32_bf16 v[56:59], v[32:35], v[194:197], v[56:59]
	v_mfma_f32_16x16x32_bf16 v[44:47], v[24:27], v[202:205], v[44:47]
	v_mfma_f32_16x16x32_bf16 v[40:43], v[32:35], v[202:205], v[40:43]
	v_mfma_f32_16x16x32_bf16 v[12:15], v[24:27], v[210:213], v[12:15]
	v_mfma_f32_16x16x32_bf16 v[8:11], v[32:35], v[210:213], v[8:11]
	v_mfma_f32_16x16x32_bf16 v[76:79], v[28:31], v[190:193], v[76:79]
	v_mfma_f32_16x16x32_bf16 v[72:75], v[36:39], v[190:193], v[72:75]
	v_mfma_f32_16x16x32_bf16 v[60:63], v[28:31], v[198:201], v[60:63]
	v_mfma_f32_16x16x32_bf16 v[56:59], v[36:39], v[198:201], v[56:59]
	v_mfma_f32_16x16x32_bf16 v[44:47], v[28:31], v[206:209], v[44:47]
	v_mfma_f32_16x16x32_bf16 v[40:43], v[36:39], v[206:209], v[40:43]
	v_mfma_f32_16x16x32_bf16 v[12:15], v[28:31], v[214:217], v[12:15]
	v_mfma_f32_16x16x32_bf16 v[8:11], v[36:39], v[214:217], v[8:11]
	v_mfma_f32_16x16x32_bf16 v[20:23], v[162:165], v[202:205], v[20:23]
	v_mfma_f32_16x16x32_bf16 v[16:19], v[178:181], v[202:205], v[16:19]
	v_mfma_f32_16x16x32_bf16 v[4:7], v[162:165], v[210:213], v[4:7]
	v_mfma_f32_16x16x32_bf16 v[0:3], v[178:181], v[210:213], v[0:3]
	v_mfma_f32_16x16x32_bf16 v[24:27], v[162:165], v[186:189], v[68:71]
	v_mfma_f32_16x16x32_bf16 v[28:31], v[178:181], v[186:189], v[64:67]
	v_mfma_f32_16x16x32_bf16 v[32:35], v[162:165], v[194:197], v[52:55]
	v_mfma_f32_16x16x32_bf16 v[36:39], v[178:181], v[194:197], v[48:51]
	v_mfma_f32_16x16x32_bf16 v[20:23], v[166:169], v[206:209], v[20:23]
	v_mfma_f32_16x16x32_bf16 v[16:19], v[182:185], v[206:209], v[16:19]
	v_mfma_f32_16x16x32_bf16 v[4:7], v[166:169], v[214:217], v[4:7]
	v_mfma_f32_16x16x32_bf16 v[0:3], v[182:185], v[214:217], v[0:3]
	v_mfma_f32_16x16x32_bf16 v[24:27], v[166:169], v[190:193], v[24:27]
	v_mfma_f32_16x16x32_bf16 v[28:31], v[182:185], v[190:193], v[28:31]
	v_mfma_f32_16x16x32_bf16 v[32:35], v[166:169], v[198:201], v[32:35]
	v_mfma_f32_16x16x32_bf16 v[36:39], v[182:185], v[198:201], v[36:39]
	s_setprio 0
	s_nop 0
	s_nop 0
	s_barrier
	s_add_i32 s70, 0, 0x18000
	s_add_i32 s71, 0, 0x1c000
	v_add_u32_e32 v68, s70, v172
	v_add_u32_e32 v152, s71, v172
	ds_read_b128 v[48:51], v68
	ds_read_b128 v[52:55], v68 offset:1024
	ds_read_b128 v[64:67], v68 offset:2048
	ds_read_b128 v[68:71], v68 offset:3072
	ds_read_b128 v[162:165], v152
	ds_read_b128 v[166:169], v152 offset:1024
	ds_read_b128 v[178:181], v152 offset:2048
	ds_read_b128 v[182:185], v152 offset:3072
	s_add_u32 s10, s10, 0x80000
	s_addc_u32 s11, s11, 0
	s_mov_b32 m0, s55
	v_lshl_add_u64 v[224:225], s[10:11], 0, v[144:145]
	ds_read_b128 v[186:189], v175 offset:32768
	ds_read_b128 v[190:193], v175 offset:33792
	ds_read_b128 v[194:197], v175 offset:34816
	ds_read_b128 v[198:201], v175 offset:35840
	ds_read_b128 v[202:205], v175 offset:36864
	ds_read_b128 v[206:209], v175 offset:37888
	ds_read_b128 v[210:213], v175 offset:38912
	ds_read_b128 v[214:217], v175 offset:39936
	global_load_lds_dwordx4 v[224:225], off
	v_lshl_add_u64 v[224:225], s[10:11], 0, v[148:149]
	s_mov_b32 m0, s57
	s_nop 0
	global_load_lds_dwordx4 v[224:225], off
	s_waitcnt vmcnt(8)
	s_waitcnt lgkmcnt(0)
	s_barrier
	s_setprio 1
	s_waitcnt lgkmcnt(0)
	v_mfma_f32_16x16x32_bf16 v[140:143], v[48:51], v[186:189], v[140:143]
	v_mfma_f32_16x16x32_bf16 v[136:139], v[64:67], v[186:189], v[136:139]
	v_mfma_f32_16x16x32_bf16 v[124:127], v[48:51], v[194:197], v[124:127]
	v_mfma_f32_16x16x32_bf16 v[120:123], v[64:67], v[194:197], v[120:123]
	v_mfma_f32_16x16x32_bf16 v[108:111], v[48:51], v[202:205], v[108:111]
	v_mfma_f32_16x16x32_bf16 v[104:107], v[64:67], v[202:205], v[104:107]
	v_mfma_f32_16x16x32_bf16 v[92:95], v[48:51], v[210:213], v[92:95]
	v_mfma_f32_16x16x32_bf16 v[88:91], v[64:67], v[210:213], v[88:91]
	v_mfma_f32_16x16x32_bf16 v[140:143], v[52:55], v[190:193], v[140:143]
	v_mfma_f32_16x16x32_bf16 v[136:139], v[68:71], v[190:193], v[136:139]
	v_mfma_f32_16x16x32_bf16 v[124:127], v[52:55], v[198:201], v[124:127]
	v_mfma_f32_16x16x32_bf16 v[120:123], v[68:71], v[198:201], v[120:123]
	v_mfma_f32_16x16x32_bf16 v[108:111], v[52:55], v[206:209], v[108:111]
	v_mfma_f32_16x16x32_bf16 v[104:107], v[68:71], v[206:209], v[104:107]
	v_mfma_f32_16x16x32_bf16 v[92:95], v[52:55], v[214:217], v[92:95]
	v_mfma_f32_16x16x32_bf16 v[88:91], v[68:71], v[214:217], v[88:91]
	v_mfma_f32_16x16x32_bf16 v[132:135], v[162:165], v[186:189], v[132:135]
	v_mfma_f32_16x16x32_bf16 v[128:131], v[178:181], v[186:189], v[128:131]
	v_mfma_f32_16x16x32_bf16 v[116:119], v[162:165], v[194:197], v[116:119]
	v_mfma_f32_16x16x32_bf16 v[112:115], v[178:181], v[194:197], v[112:115]
	v_mfma_f32_16x16x32_bf16 v[100:103], v[162:165], v[202:205], v[100:103]
	v_mfma_f32_16x16x32_bf16 v[96:99], v[178:181], v[202:205], v[96:99]
	v_mfma_f32_16x16x32_bf16 v[84:87], v[162:165], v[210:213], v[84:87]
	v_mfma_f32_16x16x32_bf16 v[80:83], v[178:181], v[210:213], v[80:83]
	v_mfma_f32_16x16x32_bf16 v[132:135], v[166:169], v[190:193], v[132:135]
	v_mfma_f32_16x16x32_bf16 v[128:131], v[182:185], v[190:193], v[128:131]
	v_mfma_f32_16x16x32_bf16 v[116:119], v[166:169], v[198:201], v[116:119]
	v_mfma_f32_16x16x32_bf16 v[112:115], v[182:185], v[198:201], v[112:115]
	v_mfma_f32_16x16x32_bf16 v[100:103], v[166:169], v[206:209], v[100:103]
	v_mfma_f32_16x16x32_bf16 v[96:99], v[182:185], v[206:209], v[96:99]
	v_mfma_f32_16x16x32_bf16 v[84:87], v[166:169], v[214:217], v[84:87]
	v_mfma_f32_16x16x32_bf16 v[80:83], v[182:185], v[214:217], v[80:83]
	s_setprio 0
	s_nop 0
	s_nop 0
	s_barrier
	s_add_i32 s10, s70, s38
	v_lshl_add_u64 v[170:171], v[170:171], 0, s[40:41]
	s_mov_b32 m0, s10
	ds_read_b128 v[186:189], v175 offset:49152
	ds_read_b128 v[190:193], v175 offset:50176
	ds_read_b128 v[194:197], v175 offset:51200
	ds_read_b128 v[198:201], v175 offset:52224
	ds_read_b128 v[202:205], v175 offset:53248
	ds_read_b128 v[206:209], v175 offset:54272
	ds_read_b128 v[210:213], v175 offset:55296
	ds_read_b128 v[214:217], v175 offset:56320
	global_load_lds_dwordx4 v[170:171], off
	s_add_i32 m0, s10, 0x2000
	s_add_u32 s8, s8, 0x80080
	v_lshl_add_u64 v[170:171], v[218:219], 0, s[40:41]
	s_addc_u32 s9, s9, 0
	s_add_i32 s10, s71, s38
	global_load_lds_dwordx4 v[170:171], off
	v_lshl_add_u64 v[170:171], s[8:9], 0, v[146:147]
	s_mov_b32 m0, s10
	s_nop 0
	global_load_lds_dwordx4 v[170:171], off
	v_lshl_add_u64 v[170:171], s[8:9], 0, v[150:151]
	s_add_i32 m0, s10, 0x2000
	s_nop 0
	global_load_lds_dwordx4 v[170:171], off
	v_lshl_add_u64 v[170:171], v[220:221], 0, s[40:41]
	s_mov_b32 m0, s76
	s_nop 0
	global_load_lds_dwordx4 v[170:171], off
	v_lshl_add_u64 v[170:171], v[222:223], 0, s[40:41]
	s_mov_b32 m0, s77
	s_nop 0
	global_load_lds_dwordx4 v[170:171], off
	s_waitcnt vmcnt(8)
	s_waitcnt lgkmcnt(0)
	s_barrier
	s_setprio 1
	s_waitcnt lgkmcnt(0)
	v_mfma_f32_16x16x32_bf16 v[76:79], v[48:51], v[186:189], v[76:79]
	v_mfma_f32_16x16x32_bf16 v[72:75], v[64:67], v[186:189], v[72:75]
	v_mfma_f32_16x16x32_bf16 v[60:63], v[48:51], v[194:197], v[60:63]
	v_mfma_f32_16x16x32_bf16 v[56:59], v[64:67], v[194:197], v[56:59]
	v_mfma_f32_16x16x32_bf16 v[44:47], v[48:51], v[202:205], v[44:47]
	v_mfma_f32_16x16x32_bf16 v[40:43], v[64:67], v[202:205], v[40:43]
	v_mfma_f32_16x16x32_bf16 v[12:15], v[48:51], v[210:213], v[12:15]
	v_mfma_f32_16x16x32_bf16 v[8:11], v[64:67], v[210:213], v[8:11]
	v_mfma_f32_16x16x32_bf16 v[76:79], v[52:55], v[190:193], v[76:79]
	v_mfma_f32_16x16x32_bf16 v[72:75], v[68:71], v[190:193], v[72:75]
	v_mfma_f32_16x16x32_bf16 v[60:63], v[52:55], v[198:201], v[60:63]
	v_mfma_f32_16x16x32_bf16 v[56:59], v[68:71], v[198:201], v[56:59]
	v_mfma_f32_16x16x32_bf16 v[44:47], v[52:55], v[206:209], v[44:47]
	v_mfma_f32_16x16x32_bf16 v[40:43], v[68:71], v[206:209], v[40:43]
	v_mfma_f32_16x16x32_bf16 v[12:15], v[52:55], v[214:217], v[12:15]
	v_mfma_f32_16x16x32_bf16 v[8:11], v[68:71], v[214:217], v[8:11]
	v_mfma_f32_16x16x32_bf16 v[24:27], v[162:165], v[186:189], v[24:27]
	v_mfma_f32_16x16x32_bf16 v[68:71], v[166:169], v[190:193], v[24:27]
	v_mfma_f32_16x16x32_bf16 v[24:27], v[178:181], v[186:189], v[28:31]
	v_mfma_f32_16x16x32_bf16 v[64:67], v[182:185], v[190:193], v[24:27]
	v_mfma_f32_16x16x32_bf16 v[24:27], v[162:165], v[194:197], v[32:35]
	v_mfma_f32_16x16x32_bf16 v[52:55], v[166:169], v[198:201], v[24:27]
	v_mfma_f32_16x16x32_bf16 v[24:27], v[178:181], v[194:197], v[36:39]
	v_mfma_f32_16x16x32_bf16 v[20:23], v[162:165], v[202:205], v[20:23]
	v_mfma_f32_16x16x32_bf16 v[16:19], v[178:181], v[202:205], v[16:19]
	v_mfma_f32_16x16x32_bf16 v[4:7], v[162:165], v[210:213], v[4:7]
	v_mfma_f32_16x16x32_bf16 v[0:3], v[178:181], v[210:213], v[0:3]
	v_mfma_f32_16x16x32_bf16 v[48:51], v[182:185], v[198:201], v[24:27]
	v_mfma_f32_16x16x32_bf16 v[20:23], v[166:169], v[206:209], v[20:23]
	v_mfma_f32_16x16x32_bf16 v[16:19], v[182:185], v[206:209], v[16:19]
	v_mfma_f32_16x16x32_bf16 v[4:7], v[166:169], v[214:217], v[4:7]
	v_mfma_f32_16x16x32_bf16 v[0:3], v[182:185], v[214:217], v[0:3]
	s_setprio 0
	s_nop 0
	s_nop 0
	s_add_i32 s65, s65, 2
	s_add_u32 s6, s6, 0x100
	s_addc_u32 s7, s7, 0
	s_add_u32 s5, s5, 0x100
	s_addc_u32 s63, s63, 0
	s_cmp_gt_u32 s65, 29
	s_barrier
	s_cbranch_scc0 .LBB0_510
	s_and_b64 vcc, exec, s[42:43]
	s_cbranch_vccz .LBB0_513
	s_barrier

.LBB0_881:
	ds_read_b128 v[144:147], v151
	ds_read_b128 v[156:159], v151 offset:1024
	ds_read_b128 v[160:163], v151 offset:2048
	ds_read_b128 v[164:167], v151 offset:3072
	ds_read_b128 v[168:171], v152
	ds_read_b128 v[172:175], v152 offset:1024
	ds_read_b128 v[176:179], v152 offset:2048
	ds_read_b128 v[180:183], v152 offset:3072
	s_add_u32 s30, s34, 0xfffc0080
	s_addc_u32 s31, s35, -1
	s_cmp_eq_u32 s56, 12
	s_cselect_b32 s37, s25, s31
	s_cselect_b32 s36, s24, s30
	s_cselect_b32 s31, s27, s23
	s_cselect_b32 s30, s26, s21
	v_lshl_add_u64 v[148:149], s[34:35], 0, v[136:137]
	s_add_i32 m0, s29, 0xc000
	ds_read_b128 v[184:187], v153
	ds_read_b128 v[188:191], v153 offset:1024
	ds_read_b128 v[192:195], v153 offset:2048
	ds_read_b128 v[196:199], v153 offset:3072
	ds_read_b128 v[200:203], v153 offset:4096
	ds_read_b128 v[204:207], v153 offset:5120
	ds_read_b128 v[208:211], v153 offset:6144
	ds_read_b128 v[212:215], v153 offset:7168
	global_load_lds_dwordx4 v[148:149], off
	v_lshl_add_u64 v[148:149], s[34:35], 0, v[138:139]
	s_add_i32 m0, s29, 0xe000
	s_nop 0
	global_load_lds_dwordx4 v[148:149], off
	s_waitcnt vmcnt(8)
	s_waitcnt lgkmcnt(0)
	s_barrier
	s_setprio 1
	s_waitcnt lgkmcnt(0)
	v_mfma_f32_16x16x32_bf16 v[124:127], v[144:147], v[184:187], v[124:127]
	v_mfma_f32_16x16x32_bf16 v[120:123], v[160:163], v[184:187], v[120:123]
	v_mfma_f32_16x16x32_bf16 v[108:111], v[144:147], v[192:195], v[108:111]
	v_mfma_f32_16x16x32_bf16 v[104:107], v[160:163], v[192:195], v[104:107]
	v_mfma_f32_16x16x32_bf16 v[92:95], v[144:147], v[200:203], v[92:95]
	v_mfma_f32_16x16x32_bf16 v[88:91], v[160:163], v[200:203], v[88:91]
	v_mfma_f32_16x16x32_bf16 v[76:79], v[144:147], v[208:211], v[76:79]
	v_mfma_f32_16x16x32_bf16 v[72:75], v[160:163], v[208:211], v[72:75]
	v_mfma_f32_16x16x32_bf16 v[124:127], v[156:159], v[188:191], v[124:127]
	v_mfma_f32_16x16x32_bf16 v[120:123], v[164:167], v[188:191], v[120:123]
	v_mfma_f32_16x16x32_bf16 v[108:111], v[156:159], v[196:199], v[108:111]
	v_mfma_f32_16x16x32_bf16 v[104:107], v[164:167], v[196:199], v[104:107]
	v_mfma_f32_16x16x32_bf16 v[92:95], v[156:159], v[204:207], v[92:95]
	v_mfma_f32_16x16x32_bf16 v[88:91], v[164:167], v[204:207], v[88:91]
	v_mfma_f32_16x16x32_bf16 v[76:79], v[156:159], v[212:215], v[76:79]
	v_mfma_f32_16x16x32_bf16 v[72:75], v[164:167], v[212:215], v[72:75]
	v_mfma_f32_16x16x32_bf16 v[116:119], v[168:171], v[184:187], v[116:119]
	v_mfma_f32_16x16x32_bf16 v[112:115], v[176:179], v[184:187], v[112:115]
	v_mfma_f32_16x16x32_bf16 v[100:103], v[168:171], v[192:195], v[100:103]
	v_mfma_f32_16x16x32_bf16 v[96:99], v[176:179], v[192:195], v[96:99]
	v_mfma_f32_16x16x32_bf16 v[84:87], v[168:171], v[200:203], v[84:87]
	v_mfma_f32_16x16x32_bf16 v[80:83], v[176:179], v[200:203], v[80:83]
	v_mfma_f32_16x16x32_bf16 v[68:71], v[168:171], v[208:211], v[68:71]
	v_mfma_f32_16x16x32_bf16 v[64:67], v[176:179], v[208:211], v[64:67]
	v_mfma_f32_16x16x32_bf16 v[116:119], v[172:175], v[188:191], v[116:119]
	v_mfma_f32_16x16x32_bf16 v[112:115], v[180:183], v[188:191], v[112:115]
	v_mfma_f32_16x16x32_bf16 v[100:103], v[172:175], v[196:199], v[100:103]
	v_mfma_f32_16x16x32_bf16 v[96:99], v[180:183], v[196:199], v[96:99]
	v_mfma_f32_16x16x32_bf16 v[84:87], v[172:175], v[204:207], v[84:87]
	v_mfma_f32_16x16x32_bf16 v[80:83], v[180:183], v[204:207], v[80:83]
	v_mfma_f32_16x16x32_bf16 v[68:71], v[172:175], v[212:215], v[68:71]
	v_mfma_f32_16x16x32_bf16 v[64:67], v[180:183], v[212:215], v[64:67]
	s_setprio 0
	s_nop 0
	s_nop 0
	s_barrier
	s_add_i32 s57, s51, s38
	v_lshl_add_u64 v[148:149], s[30:31], 0, v[130:131]
	s_mov_b32 m0, s57
	ds_read_b128 v[184:187], v153 offset:16384
	ds_read_b128 v[188:191], v153 offset:17408
	ds_read_b128 v[192:195], v153 offset:18432
	ds_read_b128 v[196:199], v153 offset:19456
	ds_read_b128 v[200:203], v153 offset:20480
	ds_read_b128 v[204:207], v153 offset:21504
	ds_read_b128 v[208:211], v153 offset:22528
	ds_read_b128 v[212:215], v153 offset:23552
	global_load_lds_dwordx4 v[148:149], off
	s_add_i32 m0, s57, 0x2000
	s_add_u32 s58, s30, 0x40000
	v_lshl_add_u64 v[216:217], s[30:31], 0, v[134:135]
	s_addc_u32 s59, s31, 0
	s_add_i32 s57, s52, s38
	global_load_lds_dwordx4 v[216:217], off
	v_lshl_add_u64 v[218:219], s[58:59], 0, v[130:131]
	s_mov_b32 m0, s57
	v_lshl_add_u64 v[220:221], s[36:37], 0, v[132:133]
	global_load_lds_dwordx4 v[218:219], off
	v_lshl_add_u64 v[218:219], s[58:59], 0, v[134:135]
	s_add_i32 m0, s57, 0x2000
	s_nop 0
	global_load_lds_dwordx4 v[218:219], off
	v_lshl_add_u64 v[218:219], s[36:37], 0, v[128:129]
	s_mov_b32 m0, s29
	s_nop 0
	global_load_lds_dwordx4 v[218:219], off
	s_mov_b32 m0, s44
	s_nop 0
	global_load_lds_dwordx4 v[220:221], off
	s_waitcnt vmcnt(8)
	s_waitcnt lgkmcnt(0)
	s_barrier
	s_setprio 1
	s_waitcnt lgkmcnt(0)
	v_mfma_f32_16x16x32_bf16 v[60:63], v[144:147], v[184:187], v[60:63]
	v_mfma_f32_16x16x32_bf16 v[56:59], v[160:163], v[184:187], v[56:59]
	v_mfma_f32_16x16x32_bf16 v[44:47], v[144:147], v[192:195], v[44:47]
	v_mfma_f32_16x16x32_bf16 v[40:43], v[160:163], v[192:195], v[40:43]
	v_mfma_f32_16x16x32_bf16 v[28:31], v[144:147], v[200:203], v[28:31]
	v_mfma_f32_16x16x32_bf16 v[24:27], v[160:163], v[200:203], v[24:27]
	v_mfma_f32_16x16x32_bf16 v[12:15], v[144:147], v[208:211], v[12:15]
	v_mfma_f32_16x16x32_bf16 v[8:11], v[160:163], v[208:211], v[8:11]
	v_mfma_f32_16x16x32_bf16 v[60:63], v[156:159], v[188:191], v[60:63]
	v_mfma_f32_16x16x32_bf16 v[56:59], v[164:167], v[188:191], v[56:59]
	v_mfma_f32_16x16x32_bf16 v[44:47], v[156:159], v[196:199], v[44:47]
	v_mfma_f32_16x16x32_bf16 v[40:43], v[164:167], v[196:199], v[40:43]
	v_mfma_f32_16x16x32_bf16 v[28:31], v[156:159], v[204:207], v[28:31]
	v_mfma_f32_16x16x32_bf16 v[24:27], v[164:167], v[204:207], v[24:27]
	v_mfma_f32_16x16x32_bf16 v[12:15], v[156:159], v[212:215], v[12:15]
	v_mfma_f32_16x16x32_bf16 v[8:11], v[164:167], v[212:215], v[8:11]
	v_mfma_f32_16x16x32_bf16 v[52:55], v[168:171], v[184:187], v[52:55]
	v_mfma_f32_16x16x32_bf16 v[48:51], v[176:179], v[184:187], v[48:51]
	v_mfma_f32_16x16x32_bf16 v[36:39], v[168:171], v[192:195], v[36:39]
	v_mfma_f32_16x16x32_bf16 v[32:35], v[176:179], v[192:195], v[32:35]
	v_mfma_f32_16x16x32_bf16 v[20:23], v[168:171], v[200:203], v[20:23]
	v_mfma_f32_16x16x32_bf16 v[16:19], v[176:179], v[200:203], v[16:19]
	v_mfma_f32_16x16x32_bf16 v[4:7], v[168:171], v[208:211], v[4:7]
	v_mfma_f32_16x16x32_bf16 v[0:3], v[176:179], v[208:211], v[0:3]
	v_mfma_f32_16x16x32_bf16 v[52:55], v[172:175], v[188:191], v[52:55]
	v_mfma_f32_16x16x32_bf16 v[48:51], v[180:183], v[188:191], v[48:51]
	v_mfma_f32_16x16x32_bf16 v[36:39], v[172:175], v[196:199], v[36:39]
	v_mfma_f32_16x16x32_bf16 v[32:35], v[180:183], v[196:199], v[32:35]
	v_mfma_f32_16x16x32_bf16 v[20:23], v[172:175], v[204:207], v[20:23]
	v_mfma_f32_16x16x32_bf16 v[16:19], v[180:183], v[204:207], v[16:19]
	v_mfma_f32_16x16x32_bf16 v[4:7], v[172:175], v[212:215], v[4:7]
	v_mfma_f32_16x16x32_bf16 v[0:3], v[180:183], v[212:215], v[0:3]
	s_setprio 0
	s_nop 0
	s_nop 0
	s_barrier
	s_add_i32 s57, 0, 0x18000
	v_add_u32_e32 v155, s57, v150
	s_add_i32 s58, 0, 0x1c000
	ds_read_b128 v[144:147], v155
	ds_read_b128 v[156:159], v155 offset:1024
	ds_read_b128 v[160:163], v155 offset:2048
	ds_read_b128 v[164:167], v155 offset:3072
	v_add_u32_e32 v155, s58, v150
	ds_read_b128 v[168:171], v155
	ds_read_b128 v[172:175], v155 offset:1024
	ds_read_b128 v[176:179], v155 offset:2048
	ds_read_b128 v[180:183], v155 offset:3072
	s_add_u32 s36, s36, 0x40000
	s_addc_u32 s37, s37, 0
	s_mov_b32 m0, s45
	v_lshl_add_u64 v[222:223], s[36:37], 0, v[128:129]
	ds_read_b128 v[184:187], v153 offset:32768
	ds_read_b128 v[188:191], v153 offset:33792
	ds_read_b128 v[192:195], v153 offset:34816
	ds_read_b128 v[196:199], v153 offset:35840
	ds_read_b128 v[200:203], v153 offset:36864
	ds_read_b128 v[204:207], v153 offset:37888
	ds_read_b128 v[208:211], v153 offset:38912
	ds_read_b128 v[212:215], v153 offset:39936
	global_load_lds_dwordx4 v[222:223], off
	v_lshl_add_u64 v[222:223], s[36:37], 0, v[132:133]
	s_mov_b32 m0, s48
	s_nop 0
	global_load_lds_dwordx4 v[222:223], off
	s_waitcnt vmcnt(8)
	s_waitcnt lgkmcnt(0)
	s_barrier
	s_setprio 1
	s_waitcnt lgkmcnt(0)
	v_mfma_f32_16x16x32_bf16 v[124:127], v[144:147], v[184:187], v[124:127]
	v_mfma_f32_16x16x32_bf16 v[120:123], v[160:163], v[184:187], v[120:123]
	v_mfma_f32_16x16x32_bf16 v[108:111], v[144:147], v[192:195], v[108:111]
	v_mfma_f32_16x16x32_bf16 v[104:107], v[160:163], v[192:195], v[104:107]
	v_mfma_f32_16x16x32_bf16 v[92:95], v[144:147], v[200:203], v[92:95]
	v_mfma_f32_16x16x32_bf16 v[88:91], v[160:163], v[200:203], v[88:91]
	v_mfma_f32_16x16x32_bf16 v[76:79], v[144:147], v[208:211], v[76:79]
	v_mfma_f32_16x16x32_bf16 v[72:75], v[160:163], v[208:211], v[72:75]
	v_mfma_f32_16x16x32_bf16 v[124:127], v[156:159], v[188:191], v[124:127]
	v_mfma_f32_16x16x32_bf16 v[120:123], v[164:167], v[188:191], v[120:123]
	v_mfma_f32_16x16x32_bf16 v[108:111], v[156:159], v[196:199], v[108:111]
	v_mfma_f32_16x16x32_bf16 v[104:107], v[164:167], v[196:199], v[104:107]
	v_mfma_f32_16x16x32_bf16 v[92:95], v[156:159], v[204:207], v[92:95]
	v_mfma_f32_16x16x32_bf16 v[88:91], v[164:167], v[204:207], v[88:91]
	v_mfma_f32_16x16x32_bf16 v[76:79], v[156:159], v[212:215], v[76:79]
	v_mfma_f32_16x16x32_bf16 v[72:75], v[164:167], v[212:215], v[72:75]
	v_mfma_f32_16x16x32_bf16 v[116:119], v[168:171], v[184:187], v[116:119]
	v_mfma_f32_16x16x32_bf16 v[112:115], v[176:179], v[184:187], v[112:115]
	v_mfma_f32_16x16x32_bf16 v[100:103], v[168:171], v[192:195], v[100:103]
	v_mfma_f32_16x16x32_bf16 v[96:99], v[176:179], v[192:195], v[96:99]
	v_mfma_f32_16x16x32_bf16 v[84:87], v[168:171], v[200:203], v[84:87]
	v_mfma_f32_16x16x32_bf16 v[80:83], v[176:179], v[200:203], v[80:83]
	v_mfma_f32_16x16x32_bf16 v[68:71], v[168:171], v[208:211], v[68:71]
	v_mfma_f32_16x16x32_bf16 v[64:67], v[176:179], v[208:211], v[64:67]
	v_mfma_f32_16x16x32_bf16 v[116:119], v[172:175], v[188:191], v[116:119]
	v_mfma_f32_16x16x32_bf16 v[112:115], v[180:183], v[188:191], v[112:115]
	v_mfma_f32_16x16x32_bf16 v[100:103], v[172:175], v[196:199], v[100:103]
	v_mfma_f32_16x16x32_bf16 v[96:99], v[180:183], v[196:199], v[96:99]
	v_mfma_f32_16x16x32_bf16 v[84:87], v[172:175], v[204:207], v[84:87]
	v_mfma_f32_16x16x32_bf16 v[80:83], v[180:183], v[204:207], v[80:83]
	v_mfma_f32_16x16x32_bf16 v[68:71], v[172:175], v[212:215], v[68:71]
	v_mfma_f32_16x16x32_bf16 v[64:67], v[180:183], v[212:215], v[64:67]
	s_setprio 0
	s_nop 0
	s_nop 0
	s_barrier
	s_add_i32 s36, s57, s38
	v_lshl_add_u64 v[148:149], v[148:149], 0, s[12:13]
	s_mov_b32 m0, s36
	ds_read_b128 v[184:187], v153 offset:49152
	ds_read_b128 v[188:191], v153 offset:50176
	ds_read_b128 v[192:195], v153 offset:51200
	ds_read_b128 v[196:199], v153 offset:52224
	ds_read_b128 v[200:203], v153 offset:53248
	ds_read_b128 v[204:207], v153 offset:54272
	ds_read_b128 v[208:211], v153 offset:55296
	ds_read_b128 v[212:215], v153 offset:56320
	global_load_lds_dwordx4 v[148:149], off
	s_add_i32 m0, s36, 0x2000
	s_add_u32 s30, s30, 0x40080
	v_lshl_add_u64 v[148:149], v[216:217], 0, s[12:13]
	s_addc_u32 s31, s31, 0
	s_add_i32 s36, s58, s38
	global_load_lds_dwordx4 v[148:149], off
	v_lshl_add_u64 v[148:149], s[30:31], 0, v[130:131]
	s_mov_b32 m0, s36
	s_nop 0
	global_load_lds_dwordx4 v[148:149], off
	v_lshl_add_u64 v[148:149], s[30:31], 0, v[134:135]
	s_add_i32 m0, s36, 0x2000
	s_nop 0
	global_load_lds_dwordx4 v[148:149], off
	v_lshl_add_u64 v[148:149], v[218:219], 0, s[12:13]
	s_mov_b32 m0, s47
	s_nop 0
	global_load_lds_dwordx4 v[148:149], off
	v_lshl_add_u64 v[148:149], v[220:221], 0, s[12:13]
	s_mov_b32 m0, s50
	s_nop 0
	global_load_lds_dwordx4 v[148:149], off
	s_waitcnt vmcnt(8)
	s_waitcnt lgkmcnt(0)
	s_barrier
	s_setprio 1
	s_waitcnt lgkmcnt(0)
	v_mfma_f32_16x16x32_bf16 v[60:63], v[144:147], v[184:187], v[60:63]
	v_mfma_f32_16x16x32_bf16 v[56:59], v[160:163], v[184:187], v[56:59]
	v_mfma_f32_16x16x32_bf16 v[44:47], v[144:147], v[192:195], v[44:47]
	v_mfma_f32_16x16x32_bf16 v[40:43], v[160:163], v[192:195], v[40:43]
	v_mfma_f32_16x16x32_bf16 v[28:31], v[144:147], v[200:203], v[28:31]
	v_mfma_f32_16x16x32_bf16 v[24:27], v[160:163], v[200:203], v[24:27]
	v_mfma_f32_16x16x32_bf16 v[12:15], v[144:147], v[208:211], v[12:15]
	v_mfma_f32_16x16x32_bf16 v[8:11], v[160:163], v[208:211], v[8:11]
	v_mfma_f32_16x16x32_bf16 v[60:63], v[156:159], v[188:191], v[60:63]
	v_mfma_f32_16x16x32_bf16 v[56:59], v[164:167], v[188:191], v[56:59]
	v_mfma_f32_16x16x32_bf16 v[44:47], v[156:159], v[196:199], v[44:47]
	v_mfma_f32_16x16x32_bf16 v[40:43], v[164:167], v[196:199], v[40:43]
	v_mfma_f32_16x16x32_bf16 v[28:31], v[156:159], v[204:207], v[28:31]
	v_mfma_f32_16x16x32_bf16 v[24:27], v[164:167], v[204:207], v[24:27]
	v_mfma_f32_16x16x32_bf16 v[12:15], v[156:159], v[212:215], v[12:15]
	v_mfma_f32_16x16x32_bf16 v[8:11], v[164:167], v[212:215], v[8:11]
	v_mfma_f32_16x16x32_bf16 v[52:55], v[168:171], v[184:187], v[52:55]
	v_mfma_f32_16x16x32_bf16 v[48:51], v[176:179], v[184:187], v[48:51]
	v_mfma_f32_16x16x32_bf16 v[36:39], v[168:171], v[192:195], v[36:39]
	v_mfma_f32_16x16x32_bf16 v[32:35], v[176:179], v[192:195], v[32:35]
	v_mfma_f32_16x16x32_bf16 v[20:23], v[168:171], v[200:203], v[20:23]
	v_mfma_f32_16x16x32_bf16 v[16:19], v[176:179], v[200:203], v[16:19]
	v_mfma_f32_16x16x32_bf16 v[4:7], v[168:171], v[208:211], v[4:7]
	v_mfma_f32_16x16x32_bf16 v[0:3], v[176:179], v[208:211], v[0:3]
	v_mfma_f32_16x16x32_bf16 v[52:55], v[172:175], v[188:191], v[52:55]
	v_mfma_f32_16x16x32_bf16 v[48:51], v[180:183], v[188:191], v[48:51]
	v_mfma_f32_16x16x32_bf16 v[36:39], v[172:175], v[196:199], v[36:39]
	v_mfma_f32_16x16x32_bf16 v[32:35], v[180:183], v[196:199], v[32:35]
	v_mfma_f32_16x16x32_bf16 v[20:23], v[172:175], v[204:207], v[20:23]
	v_mfma_f32_16x16x32_bf16 v[16:19], v[180:183], v[204:207], v[16:19]
	v_mfma_f32_16x16x32_bf16 v[4:7], v[172:175], v[212:215], v[4:7]
	v_mfma_f32_16x16x32_bf16 v[0:3], v[180:183], v[212:215], v[0:3]
	s_setprio 0
	s_nop 0
	s_nop 0
	s_add_i32 s56, s56, 2
	s_add_u32 s34, s34, 0x100
	s_addc_u32 s35, s35, 0
	s_add_u32 s21, s21, 0x100
	s_addc_u32 s23, s23, 0
	s_cmp_gt_u32 s56, 13
	s_barrier
	s_cbranch_scc0 .LBB0_881
	s_and_b64 vcc, exec, s[14:15]
	s_cbranch_vccz .LBB0_884
	s_barrier

.Lpeel5_sub3:
	s_add_i32 s39, 0, 0x18000
	s_add_i32 s60, 0, 0x1c000
	v_add_u32_e32 v12, s39, v184
	v_add_u32_e32 v28, s60, v184
	ds_read_b128 v[0:3], v12
	ds_read_b128 v[4:7], v12 offset:1024
	ds_read_b128 v[8:11], v12 offset:2048
	ds_read_b128 v[12:15], v12 offset:3072
	ds_read_b128 v[16:19], v28
	ds_read_b128 v[20:23], v28 offset:1024
	ds_read_b128 v[24:27], v28 offset:2048
	ds_read_b128 v[28:31], v28 offset:3072
	s_add_u32 s36, s36, 0x40000
	s_addc_u32 s37, s37, 0
	s_mov_b32 m0, s49
	v_lshl_add_u64 v[220:221], s[36:37], 0, v[160:161]
	ds_read_b128 v[188:191], v187 offset:32768
	ds_read_b128 v[192:195], v187 offset:33792
	ds_read_b128 v[196:199], v187 offset:34816
	ds_read_b128 v[200:203], v187 offset:35840
	ds_read_b128 v[204:207], v187 offset:36864
	ds_read_b128 v[208:211], v187 offset:37888
	ds_read_b128 v[212:215], v187 offset:38912
	ds_read_b128 v[216:219], v187 offset:39936
	global_load_lds_dwordx4 v[220:221], off
	v_lshl_add_u64 v[220:221], s[36:37], 0, v[164:165]
	s_mov_b32 m0, s50
	s_nop 0
	global_load_lds_dwordx4 v[220:221], off
	s_waitcnt vmcnt(8)
	s_waitcnt lgkmcnt(0)
	s_barrier
	s_setprio 1
	s_waitcnt lgkmcnt(0)
	v_mfma_f32_16x16x128_f8f6f4 v[156:159], v[0:7], v[188:195], v[156:159]
	v_mfma_f32_16x16x128_f8f6f4 v[152:155], v[8:15], v[188:195], v[152:155]
	v_mfma_f32_16x16x128_f8f6f4 v[140:143], v[0:7], v[196:203], v[140:143]
	v_mfma_f32_16x16x128_f8f6f4 v[136:139], v[8:15], v[196:203], v[136:139]
	v_mfma_f32_16x16x128_f8f6f4 v[124:127], v[0:7], v[204:211], v[124:127]
	v_mfma_f32_16x16x128_f8f6f4 v[120:123], v[8:15], v[204:211], v[120:123]
	v_mfma_f32_16x16x128_f8f6f4 v[108:111], v[0:7], v[212:219], v[108:111]
	v_mfma_f32_16x16x128_f8f6f4 v[104:107], v[8:15], v[212:219], v[104:107]
	v_mfma_f32_16x16x128_f8f6f4 v[148:151], v[16:23], v[188:195], v[148:151]
	v_mfma_f32_16x16x128_f8f6f4 v[144:147], v[24:31], v[188:195], v[144:147]
	v_mfma_f32_16x16x128_f8f6f4 v[132:135], v[16:23], v[196:203], v[132:135]
	v_mfma_f32_16x16x128_f8f6f4 v[128:131], v[24:31], v[196:203], v[128:131]
	v_mfma_f32_16x16x128_f8f6f4 v[116:119], v[16:23], v[204:211], v[116:119]
	v_mfma_f32_16x16x128_f8f6f4 v[112:115], v[24:31], v[204:211], v[112:115]
	v_mfma_f32_16x16x128_f8f6f4 v[100:103], v[16:23], v[212:219], v[100:103]
	v_mfma_f32_16x16x128_f8f6f4 v[96:99], v[24:31], v[212:219], v[96:99]
	s_setprio 0
	s_nop 0
	s_nop 0
	s_barrier
	s_add_i32 s36, s39, s47
	v_lshl_add_u64 v[176:177], v[176:177], 0, s[10:11]
	s_mov_b32 m0, s36
	ds_read_b128 v[188:191], v187 offset:49152
	ds_read_b128 v[192:195], v187 offset:50176
	ds_read_b128 v[196:199], v187 offset:51200
	ds_read_b128 v[200:203], v187 offset:52224
	ds_read_b128 v[204:207], v187 offset:53248
	ds_read_b128 v[208:211], v187 offset:54272
	ds_read_b128 v[212:215], v187 offset:55296
	ds_read_b128 v[216:219], v187 offset:56320
	global_load_lds_dwordx4 v[176:177], off
	s_add_i32 m0, s36, 0x2000
	s_add_u32 s30, s30, 0x40080
	v_lshl_add_u64 v[176:177], v[178:179], 0, s[10:11]
	s_addc_u32 s31, s31, 0
	s_add_i32 s36, s60, s47
	global_load_lds_dwordx4 v[176:177], off
	v_lshl_add_u64 v[176:177], s[30:31], 0, v[162:163]
	s_mov_b32 m0, s36
	s_nop 0
	global_load_lds_dwordx4 v[176:177], off
	v_lshl_add_u64 v[176:177], s[30:31], 0, v[166:167]
	s_add_i32 m0, s36, 0x2000
	s_nop 0
	global_load_lds_dwordx4 v[176:177], off
	v_lshl_add_u64 v[176:177], v[180:181], 0, s[10:11]
	s_mov_b32 m0, s54
	s_nop 0
	global_load_lds_dwordx4 v[176:177], off
	v_lshl_add_u64 v[176:177], v[182:183], 0, s[10:11]
	s_mov_b32 m0, s55
	s_nop 0
	global_load_lds_dwordx4 v[176:177], off
	s_waitcnt vmcnt(8)
	s_waitcnt lgkmcnt(0)
	s_barrier
	s_setprio 1
	s_waitcnt lgkmcnt(0)
	v_mfma_f32_16x16x128_f8f6f4 v[92:95], v[0:7], v[188:195], v[92:95]
	v_mfma_f32_16x16x128_f8f6f4 v[88:91], v[8:15], v[188:195], v[88:91]
	v_mfma_f32_16x16x128_f8f6f4 v[76:79], v[0:7], v[196:203], v[76:79]
	v_mfma_f32_16x16x128_f8f6f4 v[72:75], v[8:15], v[196:203], v[72:75]
	v_mfma_f32_16x16x128_f8f6f4 v[60:63], v[0:7], v[204:211], v[60:63]
	v_mfma_f32_16x16x128_f8f6f4 v[56:59], v[8:15], v[204:211], v[56:59]
	v_mfma_f32_16x16x128_f8f6f4 v[44:47], v[0:7], v[212:219], v[44:47]
	v_mfma_f32_16x16x128_f8f6f4 v[40:43], v[8:15], v[212:219], v[40:43]
	v_mfma_f32_16x16x128_f8f6f4 v[84:87], v[16:23], v[188:195], v[84:87]
	v_mfma_f32_16x16x128_f8f6f4 v[80:83], v[24:31], v[188:195], v[80:83]
	v_mfma_f32_16x16x128_f8f6f4 v[68:71], v[16:23], v[196:203], v[68:71]
	v_mfma_f32_16x16x128_f8f6f4 v[64:67], v[24:31], v[196:203], v[64:67]
	v_mfma_f32_16x16x128_f8f6f4 v[52:55], v[16:23], v[204:211], v[52:55]
	v_mfma_f32_16x16x128_f8f6f4 v[48:51], v[24:31], v[204:211], v[48:51]
	v_mfma_f32_16x16x128_f8f6f4 v[36:39], v[16:23], v[212:219], v[36:39]
	v_mfma_f32_16x16x128_f8f6f4 v[32:35], v[24:31], v[212:219], v[32:35]
	s_setprio 0
	s_nop 0
	s_nop 0
	s_add_i32 s38, s38, 2
	s_add_u32 s42, s42, 0x100
	s_addc_u32 s43, s43, 0
	s_add_u32 s25, s25, 0x100
	s_addc_u32 s27, s27, 0
	s_cmp_gt_u32 s38, 13
	s_barrier
	s_cbranch_scc0 .LBB0_958
	s_and_b64 vcc, exec, s[12:13]
	s_cbranch_vccz .LBB0_961
	s_barrier

.Lpeel8_sub3:
	s_add_i32 s64, 0, 0x18000
	s_add_i32 s65, 0, 0x1c000
	v_add_u32_e32 v12, s64, v236
	v_add_u32_e32 v28, s65, v236
	ds_read_b128 v[0:3], v12
	ds_read_b128 v[4:7], v12 offset:1024
	ds_read_b128 v[8:11], v12 offset:2048
	ds_read_b128 v[12:15], v12 offset:3072
	ds_read_b128 v[16:19], v28
	ds_read_b128 v[20:23], v28 offset:1024
	ds_read_b128 v[24:27], v28 offset:2048
	ds_read_b128 v[28:31], v28 offset:3072
	s_mov_b32 m0, s45
	v_lshl_add_u64 v[248:249], s[36:37], 0, v[216:217]
	ds_read_b128 v[40:43], v237 offset:32768
	ds_read_b128 v[44:47], v237 offset:33792
	ds_read_b128 v[48:51], v237 offset:34816
	ds_read_b128 v[52:55], v237 offset:35840
	ds_read_b128 v[56:59], v237 offset:36864
	ds_read_b128 v[60:63], v237 offset:37888
	ds_read_b128 v[240:243], v237 offset:38912
	ds_read_b128 v[244:247], v237 offset:39936
	global_load_lds_dwordx4 v[248:249], off
	v_lshl_add_u64 v[248:249], s[36:37], 0, v[218:219]
	s_mov_b32 m0, s46
	s_nop 0
	global_load_lds_dwordx4 v[248:249], off
	s_waitcnt vmcnt(8)
	s_waitcnt lgkmcnt(0)
	s_barrier
	s_setprio 1
	s_waitcnt lgkmcnt(0)
	v_mfma_f32_16x16x128_f8f6f4 v[204:207], v[0:7], v[40:47], v[204:207]
	v_mfma_f32_16x16x128_f8f6f4 v[196:199], v[8:15], v[40:47], v[196:199]
	v_mfma_f32_16x16x128_f8f6f4 v[188:191], v[0:7], v[48:55], v[188:191]
	v_mfma_f32_16x16x128_f8f6f4 v[180:183], v[8:15], v[48:55], v[180:183]
	v_mfma_f32_16x16x128_f8f6f4 v[172:175], v[0:7], v[56:63], v[172:175]
	v_mfma_f32_16x16x128_f8f6f4 v[164:167], v[8:15], v[56:63], v[164:167]
	v_mfma_f32_16x16x128_f8f6f4 v[156:159], v[0:7], v[240:247], v[156:159]
	v_mfma_f32_16x16x128_f8f6f4 v[148:151], v[8:15], v[240:247], v[148:151]
	v_mfma_f32_16x16x128_f8f6f4 v[200:203], v[16:23], v[40:47], v[200:203]
	v_mfma_f32_16x16x128_f8f6f4 v[192:195], v[24:31], v[40:47], v[192:195]
	v_mfma_f32_16x16x128_f8f6f4 v[184:187], v[16:23], v[48:55], v[184:187]
	v_mfma_f32_16x16x128_f8f6f4 v[176:179], v[24:31], v[48:55], v[176:179]
	v_mfma_f32_16x16x128_f8f6f4 v[168:171], v[16:23], v[56:63], v[168:171]
	v_mfma_f32_16x16x128_f8f6f4 v[160:163], v[24:31], v[56:63], v[160:163]
	v_mfma_f32_16x16x128_f8f6f4 v[152:155], v[16:23], v[240:247], v[152:155]
	v_mfma_f32_16x16x128_f8f6f4 v[144:147], v[24:31], v[240:247], v[144:147]
	s_setprio 0
	s_nop 0
	s_nop 0
	s_barrier
	s_add_i32 s36, s64, s38
	v_lshl_add_u64 v[34:35], v[34:35], 0, s[12:13]
	s_mov_b32 m0, s36
	ds_read_b128 v[40:43], v237 offset:49152
	ds_read_b128 v[44:47], v237 offset:50176
	ds_read_b128 v[48:51], v237 offset:51200
	ds_read_b128 v[52:55], v237 offset:52224
	ds_read_b128 v[56:59], v237 offset:53248
	ds_read_b128 v[60:63], v237 offset:54272
	ds_read_b128 v[240:243], v237 offset:55296
	ds_read_b128 v[244:247], v237 offset:56320
	global_load_lds_dwordx4 v[34:35], off
	s_add_i32 m0, s36, 0x2000
	s_add_u32 s30, s30, 0x40080
	v_lshl_add_u64 v[32:33], v[32:33], 0, s[12:13]
	s_addc_u32 s31, s31, 0
	s_add_i32 s36, s65, s38
	global_load_lds_dwordx4 v[32:33], off
	v_lshl_add_u64 v[32:33], s[30:31], 0, v[208:209]
	s_mov_b32 m0, s36
	s_nop 0
	global_load_lds_dwordx4 v[32:33], off
	v_lshl_add_u64 v[32:33], s[30:31], 0, v[210:211]
	s_add_i32 m0, s36, 0x2000
	s_nop 0
	global_load_lds_dwordx4 v[32:33], off
	v_lshl_add_u64 v[32:33], v[38:39], 0, s[12:13]
	s_mov_b32 m0, s50
	s_nop 0
	global_load_lds_dwordx4 v[32:33], off
	v_lshl_add_u64 v[32:33], v[36:37], 0, s[12:13]
	s_mov_b32 m0, s51
	s_nop 0
	global_load_lds_dwordx4 v[32:33], off
	s_waitcnt vmcnt(8)
	s_waitcnt lgkmcnt(0)
	s_barrier
	s_setprio 1
	s_waitcnt lgkmcnt(0)
	v_mfma_f32_16x16x128_f8f6f4 v[140:143], v[0:7], v[40:47], v[140:143]
	v_mfma_f32_16x16x128_f8f6f4 v[132:135], v[8:15], v[40:47], v[132:135]
	v_mfma_f32_16x16x128_f8f6f4 v[124:127], v[0:7], v[48:55], v[124:127]
	v_mfma_f32_16x16x128_f8f6f4 v[116:119], v[8:15], v[48:55], v[116:119]
	v_mfma_f32_16x16x128_f8f6f4 v[108:111], v[0:7], v[56:63], v[108:111]
	v_mfma_f32_16x16x128_f8f6f4 v[100:103], v[8:15], v[56:63], v[100:103]
	v_mfma_f32_16x16x128_f8f6f4 v[92:95], v[0:7], v[240:247], v[92:95]
	v_mfma_f32_16x16x128_f8f6f4 v[84:87], v[8:15], v[240:247], v[84:87]
	v_mfma_f32_16x16x128_f8f6f4 v[136:139], v[16:23], v[40:47], v[136:139]
	v_mfma_f32_16x16x128_f8f6f4 v[128:131], v[24:31], v[40:47], v[128:131]
	v_mfma_f32_16x16x128_f8f6f4 v[120:123], v[16:23], v[48:55], v[120:123]
	v_mfma_f32_16x16x128_f8f6f4 v[112:115], v[24:31], v[48:55], v[112:115]
	v_mfma_f32_16x16x128_f8f6f4 v[104:107], v[16:23], v[56:63], v[104:107]
	v_mfma_f32_16x16x128_f8f6f4 v[96:99], v[24:31], v[56:63], v[96:99]
	v_mfma_f32_16x16x128_f8f6f4 v[88:91], v[16:23], v[240:247], v[88:91]
	v_mfma_f32_16x16x128_f8f6f4 v[80:83], v[24:31], v[240:247], v[80:83]
	s_setprio 0
	s_nop 0
	s_nop 0
	s_add_i32 s63, s63, 2
	s_add_u32 s34, s34, 0x100
	s_addc_u32 s35, s35, 0
	s_add_u32 s23, s23, 0x100
	s_addc_u32 s29, s29, 0
	s_cmp_gt_u32 s63, 13
	s_barrier
	s_cbranch_scc1 .LBB0_1194

.Lpeel9_sub3:
	s_add_i32 s38, 0, 0x18000
	s_add_i32 s39, 0, 0x1c000
	v_add_u32_e32 v12, s38, v186
	v_add_u32_e32 v28, s39, v186
	ds_read_b128 v[0:3], v12
	ds_read_b128 v[4:7], v12 offset:1024
	ds_read_b128 v[8:11], v12 offset:2048
	ds_read_b128 v[12:15], v12 offset:3072
	ds_read_b128 v[16:19], v28
	ds_read_b128 v[20:23], v28 offset:1024
	ds_read_b128 v[24:27], v28 offset:2048
	ds_read_b128 v[28:31], v28 offset:3072
	s_add_u32 s36, s36, 0x40000
	s_addc_u32 s37, s37, 0
	s_mov_b32 m0, s64
	v_lshl_add_u64 v[222:223], s[36:37], 0, v[162:163]
	ds_read_b128 v[190:193], v187 offset:32768
	ds_read_b128 v[194:197], v187 offset:33792
	ds_read_b128 v[198:201], v187 offset:34816
	ds_read_b128 v[202:205], v187 offset:35840
	ds_read_b128 v[206:209], v187 offset:36864
	ds_read_b128 v[210:213], v187 offset:37888
	ds_read_b128 v[214:217], v187 offset:38912
	ds_read_b128 v[218:221], v187 offset:39936
	global_load_lds_dwordx4 v[222:223], off
	v_lshl_add_u64 v[222:223], s[36:37], 0, v[166:167]
	s_mov_b32 m0, s65
	s_nop 0
	global_load_lds_dwordx4 v[222:223], off
	s_waitcnt vmcnt(8)
	s_waitcnt lgkmcnt(0)
	s_barrier
	s_setprio 1
	s_waitcnt lgkmcnt(0)
	v_mfma_f32_16x16x128_f8f6f4 v[156:159], v[0:7], v[190:197], v[156:159]
	v_mfma_f32_16x16x128_f8f6f4 v[152:155], v[8:15], v[190:197], v[152:155]
	v_mfma_f32_16x16x128_f8f6f4 v[140:143], v[0:7], v[198:205], v[140:143]
	v_mfma_f32_16x16x128_f8f6f4 v[136:139], v[8:15], v[198:205], v[136:139]
	v_mfma_f32_16x16x128_f8f6f4 v[124:127], v[0:7], v[206:213], v[124:127]
	v_mfma_f32_16x16x128_f8f6f4 v[120:123], v[8:15], v[206:213], v[120:123]
	v_mfma_f32_16x16x128_f8f6f4 v[108:111], v[0:7], v[214:221], v[108:111]
	v_mfma_f32_16x16x128_f8f6f4 v[104:107], v[8:15], v[214:221], v[104:107]
	v_mfma_f32_16x16x128_f8f6f4 v[148:151], v[16:23], v[190:197], v[148:151]
	v_mfma_f32_16x16x128_f8f6f4 v[144:147], v[24:31], v[190:197], v[144:147]
	v_mfma_f32_16x16x128_f8f6f4 v[132:135], v[16:23], v[198:205], v[132:135]
	v_mfma_f32_16x16x128_f8f6f4 v[128:131], v[24:31], v[198:205], v[128:131]
	v_mfma_f32_16x16x128_f8f6f4 v[116:119], v[16:23], v[206:213], v[116:119]
	v_mfma_f32_16x16x128_f8f6f4 v[112:115], v[24:31], v[206:213], v[112:115]
	v_mfma_f32_16x16x128_f8f6f4 v[100:103], v[16:23], v[214:221], v[100:103]
	v_mfma_f32_16x16x128_f8f6f4 v[96:99], v[24:31], v[214:221], v[96:99]
	s_setprio 0
	s_nop 0
	s_nop 0
	s_barrier
	s_add_i32 s36, s38, s47
	v_lshl_add_u64 v[178:179], v[178:179], 0, s[14:15]
	s_mov_b32 m0, s36
	ds_read_b128 v[190:193], v187 offset:49152
	ds_read_b128 v[194:197], v187 offset:50176
	ds_read_b128 v[198:201], v187 offset:51200
	ds_read_b128 v[202:205], v187 offset:52224
	ds_read_b128 v[206:209], v187 offset:53248
	ds_read_b128 v[210:213], v187 offset:54272
	ds_read_b128 v[214:217], v187 offset:55296
	ds_read_b128 v[218:221], v187 offset:56320
	global_load_lds_dwordx4 v[178:179], off
	s_add_i32 m0, s36, 0x2000
	s_add_u32 s30, s30, 0x40080
	v_lshl_add_u64 v[178:179], v[180:181], 0, s[14:15]
	s_addc_u32 s31, s31, 0
	s_add_i32 s36, s39, s47
	global_load_lds_dwordx4 v[178:179], off
	v_lshl_add_u64 v[178:179], s[30:31], 0, v[164:165]
	s_mov_b32 m0, s36
	s_nop 0
	global_load_lds_dwordx4 v[178:179], off
	v_lshl_add_u64 v[178:179], s[30:31], 0, v[168:169]
	s_add_i32 m0, s36, 0x2000
	s_nop 0
	global_load_lds_dwordx4 v[178:179], off
	v_lshl_add_u64 v[178:179], v[182:183], 0, s[14:15]
	s_mov_b32 m0, s66
	s_nop 0
	global_load_lds_dwordx4 v[178:179], off
	v_lshl_add_u64 v[178:179], v[184:185], 0, s[14:15]
	s_mov_b32 m0, s67
	s_nop 0
	global_load_lds_dwordx4 v[178:179], off
	s_waitcnt vmcnt(8)
	s_waitcnt lgkmcnt(0)
	s_barrier
	s_setprio 1
	s_waitcnt lgkmcnt(0)
	v_mfma_f32_16x16x128_f8f6f4 v[92:95], v[0:7], v[190:197], v[92:95]
	v_mfma_f32_16x16x128_f8f6f4 v[88:91], v[8:15], v[190:197], v[88:91]
	v_mfma_f32_16x16x128_f8f6f4 v[76:79], v[0:7], v[198:205], v[76:79]
	v_mfma_f32_16x16x128_f8f6f4 v[72:75], v[8:15], v[198:205], v[72:75]
	v_mfma_f32_16x16x128_f8f6f4 v[60:63], v[0:7], v[206:213], v[60:63]
	v_mfma_f32_16x16x128_f8f6f4 v[56:59], v[8:15], v[206:213], v[56:59]
	v_mfma_f32_16x16x128_f8f6f4 v[44:47], v[0:7], v[214:221], v[44:47]
	v_mfma_f32_16x16x128_f8f6f4 v[40:43], v[8:15], v[214:221], v[40:43]
	v_mfma_f32_16x16x128_f8f6f4 v[84:87], v[16:23], v[190:197], v[84:87]
	v_mfma_f32_16x16x128_f8f6f4 v[80:83], v[24:31], v[190:197], v[80:83]
	v_mfma_f32_16x16x128_f8f6f4 v[68:71], v[16:23], v[198:205], v[68:71]
	v_mfma_f32_16x16x128_f8f6f4 v[64:67], v[24:31], v[198:205], v[64:67]
	v_mfma_f32_16x16x128_f8f6f4 v[52:55], v[16:23], v[206:213], v[52:55]
	v_mfma_f32_16x16x128_f8f6f4 v[48:51], v[24:31], v[206:213], v[48:51]
	v_mfma_f32_16x16x128_f8f6f4 v[36:39], v[16:23], v[214:221], v[36:39]
	v_mfma_f32_16x16x128_f8f6f4 v[32:35], v[24:31], v[214:221], v[32:35]
	s_setprio 0
	s_nop 0
	s_nop 0
	s_add_i32 s35, s35, 2
	s_add_u32 s44, s44, 0x100
	s_addc_u32 s45, s45, 0
	s_add_u32 s21, s21, 0x100
	s_addc_u32 s23, s23, 0
	s_cmp_gt_u32 s35, 13
	s_barrier
	s_cbranch_scc1 .LBB0_1273
